# grid barrier: leaders add to the cross-XCD arrival counter without waiting for the old value; every workgroup waits on that counter reaching (gen+1)*nx
# speedup vs baseline: 1.0116x; 1.0049x over previous
.LBB0_606:
	s_or_b64 exec, exec, s[4:5]
	s_waitcnt lgkmcnt(1)
	v_max_u32_e32 v5, 1, v2
	v_cvt_f32_u32_e32 v6, v5
	s_waitcnt vmcnt(0)
	v_readfirstlane_b32 s2, v4
	v_rcp_iflag_f32_e32 v6, v6
	s_nop 0
	v_add_u32_e32 v4, s2, v1
	v_sub_u32_e32 v1, 0, v5
	v_mul_f32_e32 v6, 0x4f7ffffe, v6
	v_cvt_u32_f32_e32 v6, v6
	v_mul_lo_u32 v1, v1, v6
	v_mul_hi_u32 v1, v6, v1
	v_add_u32_e32 v1, v6, v1
	v_mul_hi_u32 v1, v4, v1
	v_mul_lo_u32 v6, v1, v5
	v_sub_u32_e32 v6, v4, v6
	v_add_u32_e32 v7, 1, v1
	v_cmp_ge_u32_e32 vcc, v6, v5
	v_add_u32_e32 v4, 1, v4
	s_nop 0
	v_cndmask_b32_e32 v1, v1, v7, vcc
	v_sub_u32_e32 v7, v6, v5
	v_cndmask_b32_e32 v6, v6, v7, vcc
	v_add_u32_e32 v7, 1, v1
	v_cmp_ge_u32_e32 vcc, v6, v5
	s_nop 1
	v_cndmask_b32_e32 v1, v1, v7, vcc
	v_mul_lo_u32 v6, v5, v1
	v_add_u32_e32 v5, v6, v5
	v_cmp_ne_u32_e32 vcc, v4, v5
	s_mov_b64 s[4:5], vcc
	v_readlane_b32 s6, v253, 11
	v_readlane_b32 s7, v253, 12
	s_waitcnt lgkmcnt(0)
	v_cmp_ne_u32_e32 vcc, 0, v2
	v_add_u32_e32 v5, 1, v1
	s_nop 1
	v_cndmask_b32_e32 v6, 1, v3, vcc
	v_mul_lo_u32 v5, v5, v6
	s_and_b64 vcc, exec, s[4:5]
	s_cbranch_vccnz .Lxb_poll_0
	buffer_wbl2 sc1
	s_waitcnt vmcnt(0)
	global_atomic_add v87, v230, s[6:7]
.Lxb_poll_0:
	s_mov_b32 s8, 0
.Lxb_spin_0:
	global_load_dword v2, v87, s[6:7] sc1
	s_waitcnt vmcnt(0)
	v_cmp_le_u32_e32 vcc, v5, v2
	s_cbranch_vccnz .Lxb_done_0
	s_sleep 1
	s_add_i32 s8, s8, 1
	s_cmpk_lt_u32 s8, 0x4000
	s_cbranch_scc1 .Lxb_spin_0
.Lxb_done_0:
	buffer_inv sc1
	s_waitcnt vmcnt(0)
	s_branch .LBB0_650



.LBB0_624:
	s_or_b64 exec, exec, s[6:7]
	s_or_b64 s[4:5], vcc, s[4:5]
	s_waitcnt lgkmcnt(0)
	s_barrier
	s_and_saveexec_b64 s[2:3], s[4:5]
	s_cbranch_execz .LBB0_618
	global_load_dword v5, v[16:17], off
	v_mov_b32_e32 v2, s14
	v_mov_b32_e32 v3, s12
	v_cndmask_b32_e32 v2, v2, v3, vcc
	ds_read_b32 v3, v24
	s_mov_b32 s4, 0xbfb8aa3b
	v_lshlrev_b32_e32 v4, 4, v2
	v_ashrrev_i32_e32 v2, 3, v2
	v_and_b32_e32 v2, -16, v2
	v_add_u32_e32 v2, v2, v10
	s_waitcnt vmcnt(0) lgkmcnt(0)
	v_add_f32_e32 v3, v3, v5
	v_min_f32_e32 v5, 0, v3
	v_mul_f32_e64 v3, |v3|, s4
	v_exp_f32_e32 v3, v3
	s_movk_i32 s4, 0x7f0
	v_and_or_b32 v4, v4, s4, v1
	v_lshlrev_b32_e32 v86, 2, v4
	v_add_f32_e32 v3, 1.0, v3
	v_log_f32_e32 v3, v3
	s_nop 0
	v_fmac_f32_e32 v5, 0xbf317218, v3
	v_ashrrev_i32_e32 v3, 31, v2
	v_lshlrev_b64 v[2:3], 13, v[2:3]
	v_lshl_add_u64 v[2:3], s[8:9], 0, v[2:3]
	v_lshl_add_u64 v[2:3], v[2:3], 0, v[86:87]
	global_store_dword v[2:3], v5, off
	s_branch .LBB0_618



.Lxb_done_1:
	buffer_inv sc1
	s_waitcnt vmcnt(0)


